# grid barriers P1->P2 and P5->P6 release per XCC (consumers read same-XCC data under the XCC-even mapping)
# baseline (speedup 1.0000x reference)
.LBB0_496:
	s_andn2_saveexec_b64 s[2:3], s[6:7]
	s_cbranch_execz .LBB0_516
	s_mov_b64 s[6:7], exec
	v_mov_b32_e32 v1, 0x123f4
	ds_read_b32 v1, v1
	s_waitcnt lgkmcnt(0)
	v_readfirstlane_b32 s2, v1
	s_cmp_lg_u32 s2, 0
	s_cbranch_scc1 .LBB0_513
	buffer_wbl2 sc1
	s_waitcnt lgkmcnt(0)
	s_waitcnt vmcnt(0)
	v_mbcnt_lo_u32_b32 v1, s6, 0
	v_mbcnt_hi_u32_b32 v1, s7, v1
	v_cmp_eq_u32_e32 vcc, 0, v1
	s_and_saveexec_b64 s[8:9], vcc
	s_cbranch_execz .LBB0_499
	s_bcnt1_i32_b64 s2, s[6:7]
	v_mov_b32_e32 v4, s2
	v_readlane_b32 s2, v254, 54
	v_readlane_b32 s3, v254, 55
	s_nop 4
	global_atomic_add v4, v3, v4, s[2:3] sc0
